# attention main loop: row-max chain trimmed (no canonicalising max pairs, no +0, rescale flag preset instead of s_cmp/s_cselect behind the v_cmp)
# speedup vs baseline: 1.0148x; 1.0001x over previous
.LBB0_1028:
	v_add_u32_e32 v230, s44, v228
	ds_read_b64_tr_b16 v[190:191], v230 offset:49152
	ds_read_b64_tr_b16 v[192:193], v230 offset:49664
	s_waitcnt lgkmcnt(9)
	v_mfma_f32_32x32x16_bf16 v[114:129], v[102:105], v[158:161], v[236:251]
	v_add_f32_e32 v106, v82, v83
	v_add_f32_e32 v106, v84, v106
	v_add_f32_e32 v106, v85, v106
	v_add_f32_e32 v106, v86, v106
	v_add_f32_e32 v106, v87, v106
	v_cvt_pk_bf16_f32 v150, v82, v83
	v_cvt_pk_bf16_f32 v151, v84, v85
	ds_read_b64_tr_b16 v[186:187], v230 offset:53248
	ds_read_b64_tr_b16 v[188:189], v230 offset:53760
	v_add_f32_e32 v82, v88, v106
	s_waitcnt lgkmcnt(10)
	v_mfma_f32_32x32x16_bf16 v[98:113], v[98:101], v[158:161], v[236:251]
	v_add_f32_e32 v82, v89, v82
	v_add_f32_e32 v82, v90, v82
	v_add_f32_e32 v130, v91, v82
	v_cvt_pk_bf16_f32 v152, v86, v87
	v_cvt_pk_bf16_f32 v153, v88, v89
	ds_read_b64_tr_b16 v[82:83], v230 offset:57344
	ds_read_b64_tr_b16 v[84:85], v230 offset:57856
	s_waitcnt lgkmcnt(11)
	v_mfma_f32_32x32x16_bf16 v[114:129], v[182:185], v[154:157], v[114:129]
	v_add_f32_e32 v86, v92, v130
	v_add_f32_e32 v86, v93, v86
	v_add_f32_e32 v86, v94, v86
	v_add_f32_e32 v130, v95, v86
	v_cvt_pk_bf16_f32 v138, v90, v91
	v_cvt_pk_bf16_f32 v139, v92, v93
	ds_read_b64_tr_b16 v[86:87], v230 offset:61440
	ds_read_b64_tr_b16 v[88:89], v230 offset:61952
	s_waitcnt lgkmcnt(12)
	v_mfma_f32_32x32x16_bf16 v[98:113], v[178:181], v[154:157], v[98:113]
	v_add_f32_e32 v90, v96, v130
	v_add_f32_e32 v90, v97, v90
	v_add_f32_e32 v90, v66, v90
	v_add_f32_e32 v130, v67, v90
	v_cvt_pk_bf16_f32 v140, v94, v95
	v_cvt_pk_bf16_f32 v141, v96, v97
	ds_read_b64_tr_b16 v[90:91], v230 offset:50176
	ds_read_b64_tr_b16 v[92:93], v230 offset:50688
	s_waitcnt lgkmcnt(13)
	v_mfma_f32_32x32x16_bf16 v[114:129], v[174:177], v[146:149], v[114:129]
	v_add_f32_e32 v94, v68, v130
	v_add_f32_e32 v94, v69, v94
	v_add_f32_e32 v94, v70, v94
	v_add_f32_e32 v130, v71, v94
	v_cvt_pk_bf16_f32 v134, v66, v67
	v_cvt_pk_bf16_f32 v135, v68, v69
	ds_read_b64_tr_b16 v[94:95], v230 offset:54272
	ds_read_b64_tr_b16 v[96:97], v230 offset:54784
	s_waitcnt lgkmcnt(14)
	v_mfma_f32_32x32x16_bf16 v[98:113], v[170:173], v[146:149], v[98:113]
	v_add_f32_e32 v66, v72, v130
	v_add_f32_e32 v66, v73, v66
	v_add_f32_e32 v66, v74, v66
	v_add_f32_e32 v66, v75, v66
	v_cvt_pk_bf16_f32 v136, v70, v71
	v_cvt_pk_bf16_f32 v137, v72, v73
	ds_read_b64_tr_b16 v[194:195], v230 offset:58368
	ds_read_b64_tr_b16 v[196:197], v230 offset:58880
	s_waitcnt lgkmcnt(14)
	v_mfma_f32_32x32x16_bf16 v[114:129], v[166:169], v[142:145], v[114:129]
	v_add_f32_e32 v66, v76, v66
	v_add_f32_e32 v66, v77, v66
	v_add_f32_e32 v66, v78, v66
	v_add_f32_e32 v66, v79, v66
	v_cvt_pk_bf16_f32 v130, v74, v75
	v_cvt_pk_bf16_f32 v131, v76, v77
	ds_read_b64_tr_b16 v[74:75], v230 offset:62464
	ds_read_b64_tr_b16 v[76:77], v230 offset:62976
	v_mfma_f32_32x32x16_bf16 v[98:113], v[162:165], v[142:145], v[98:113]
	v_add_f32_e32 v66, v80, v66
	v_add_f32_e32 v66, v81, v66
	v_cvt_pk_bf16_f32 v132, v78, v79
	v_cvt_pk_bf16_f32 v133, v80, v81
	s_add_i32 s4, s10, s89
	s_mov_b32 s5, m0
	s_mov_b32 m0, s4
	s_nop 0
	global_load_lds_dwordx4 v[220:221], off
	s_mov_b32 m0, s5
	v_add_f32_e32 v234, v234, v66
	s_addk_i32 s4, 0x400
	s_mov_b32 s5, m0
	s_mov_b32 m0, s4
	s_nop 0
	global_load_lds_dwordx4 v[218:219], off
	s_mov_b32 m0, s5
	v_lshl_add_u64 v[66:67], v[224:225], 0, s[0:1]
	s_add_i32 s4, s9, s70
	s_mov_b32 s5, m0
	s_mov_b32 m0, s4
	s_nop 0
	global_load_lds_dwordx4 v[66:67], off
	s_mov_b32 m0, s5
	v_lshl_add_u64 v[66:67], v[224:225], 0, s[64:65]
	s_addk_i32 s4, 0x400
	s_mov_b32 s5, m0
	s_mov_b32 m0, s4
	s_nop 0
	global_load_lds_dwordx4 v[66:67], off
	s_mov_b32 m0, s5
	v_max_f32_e32 v66, v114, v115
	v_max3_f32 v67, v116, v117, v99
	v_max3_f32 v66, v66, v98, v100
	v_max3_f32 v66, v66, v101, v118
	v_max3_f32 v67, v67, v120, v121
	v_max3_f32 v66, v66, v119, v102
	v_max3_f32 v67, v67, v104, v105
	v_max3_f32 v66, v66, v103, v122
	v_max3_f32 v67, v67, v124, v125
	v_max3_f32 v66, v66, v123, v106
	v_max3_f32 v67, v67, v108, v109
	v_max3_f32 v66, v66, v107, v126
	v_max3_f32 v67, v67, v128, v129
	v_max3_f32 v66, v66, v127, v110
	v_max3_f32 v67, v67, v112, v113
	v_max3_f32 v66, v66, v111, v67
	v_mov_b32_e32 v67, v66
	s_nop 1
	v_permlane32_swap_b32_e32 v66, v67
	v_max_f32_e32 v66, v66, v67
	s_mov_b64 s[4:5], 0
	v_cmp_lt_f32_e32 vcc, s3, v66
	s_cbranch_vccnz .LBB0_1036

.LBB0_1031:
	s_add_i32 s4, s9, 0x4000
	s_cmpk_lg_u32 s9, 0x8000
	s_cselect_b32 s11, s4, 0
	v_add_u32_e32 v230, s10, v228
	ds_read_b64_tr_b16 v[190:191], v230 offset:49152
	ds_read_b64_tr_b16 v[192:193], v230 offset:49664
	v_mfma_f32_32x32x16_bf16 v[82:97], v[70:73], v[158:161], v[236:251]
	v_add_f32_e32 v74, v114, v115
	v_add_f32_e32 v74, v116, v74
	v_add_f32_e32 v74, v117, v74
	v_add_f32_e32 v74, v118, v74
	v_add_f32_e32 v74, v119, v74
	v_cvt_pk_bf16_f32 v150, v114, v115
	v_cvt_pk_bf16_f32 v151, v116, v117
	ds_read_b64_tr_b16 v[186:187], v230 offset:53248
	ds_read_b64_tr_b16 v[188:189], v230 offset:53760
	v_add_f32_e32 v70, v120, v74
	v_add_f32_e32 v70, v121, v70
	v_add_f32_e32 v70, v122, v70
	v_add_f32_e32 v130, v123, v70
	v_mfma_f32_32x32x16_bf16 v[66:81], v[66:69], v[158:161], v[236:251]
	v_cvt_pk_bf16_f32 v152, v118, v119
	v_cvt_pk_bf16_f32 v153, v120, v121
	ds_read_b64_tr_b16 v[114:115], v230 offset:57344
	ds_read_b64_tr_b16 v[116:117], v230 offset:57856
	v_mfma_f32_32x32x16_bf16 v[82:97], v[182:185], v[154:157], v[82:97]
	v_add_f32_e32 v118, v124, v130
	v_add_f32_e32 v118, v125, v118
	v_add_f32_e32 v118, v126, v118
	v_add_f32_e32 v130, v127, v118
	v_cvt_pk_bf16_f32 v138, v122, v123
	v_cvt_pk_bf16_f32 v139, v124, v125
	ds_read_b64_tr_b16 v[118:119], v230 offset:61440
	ds_read_b64_tr_b16 v[120:121], v230 offset:61952
	v_mfma_f32_32x32x16_bf16 v[66:81], v[178:181], v[154:157], v[66:81]
	v_add_f32_e32 v122, v128, v130
	v_add_f32_e32 v122, v129, v122
	v_add_f32_e32 v122, v98, v122
	v_add_f32_e32 v130, v99, v122
	v_cvt_pk_bf16_f32 v140, v126, v127
	v_cvt_pk_bf16_f32 v141, v128, v129
	ds_read_b64_tr_b16 v[122:123], v230 offset:50176
	ds_read_b64_tr_b16 v[124:125], v230 offset:50688
	v_mfma_f32_32x32x16_bf16 v[82:97], v[174:177], v[146:149], v[82:97]
	v_add_f32_e32 v126, v100, v130
	v_add_f32_e32 v126, v101, v126
	v_add_f32_e32 v126, v102, v126
	v_add_f32_e32 v130, v103, v126
	v_cvt_pk_bf16_f32 v134, v98, v99
	v_cvt_pk_bf16_f32 v135, v100, v101
	ds_read_b64_tr_b16 v[126:127], v230 offset:54272
	ds_read_b64_tr_b16 v[128:129], v230 offset:54784
	v_mfma_f32_32x32x16_bf16 v[66:81], v[170:173], v[146:149], v[66:81]
	v_add_f32_e32 v98, v104, v130
	v_add_f32_e32 v98, v105, v98
	v_add_f32_e32 v98, v106, v98
	v_add_f32_e32 v98, v107, v98
	v_cvt_pk_bf16_f32 v136, v102, v103
	v_cvt_pk_bf16_f32 v137, v104, v105
	ds_read_b64_tr_b16 v[194:195], v230 offset:58368
	ds_read_b64_tr_b16 v[196:197], v230 offset:58880
	v_mfma_f32_32x32x16_bf16 v[82:97], v[166:169], v[142:145], v[82:97]
	v_add_f32_e32 v98, v108, v98
	v_add_f32_e32 v98, v109, v98
	v_add_f32_e32 v98, v110, v98
	v_add_f32_e32 v98, v111, v98
	v_cvt_pk_bf16_f32 v130, v106, v107
	v_cvt_pk_bf16_f32 v131, v108, v109
	ds_read_b64_tr_b16 v[106:107], v230 offset:62464
	ds_read_b64_tr_b16 v[108:109], v230 offset:62976
	v_mfma_f32_32x32x16_bf16 v[66:81], v[162:165], v[142:145], v[66:81]
	v_add_f32_e32 v98, v112, v98
	v_add_f32_e32 v98, v113, v98
	v_cvt_pk_bf16_f32 v132, v110, v111
	v_cvt_pk_bf16_f32 v133, v112, v113
	s_nop 0
	v_add_f32_e32 v234, v234, v98
	s_add_i32 s4, s9, s89
	v_lshl_add_u64 v[98:99], v[220:221], 0, s[0:1]
	s_mov_b32 s5, m0
	s_mov_b32 m0, s4
	s_nop 0
	global_load_lds_dwordx4 v[98:99], off
	s_mov_b32 m0, s5
	v_lshl_add_u64 v[98:99], v[218:219], 0, s[0:1]
	s_addk_i32 s4, 0x400
	s_mov_b32 s5, m0
	s_mov_b32 m0, s4
	s_nop 0
	global_load_lds_dwordx4 v[98:99], off
	s_mov_b32 m0, s5
	v_lshl_add_u64 v[110:111], v[224:225], 0, s[74:75]
	s_add_i32 s4, s11, s70
	s_mov_b32 s5, m0
	s_mov_b32 m0, s4
	s_nop 0
	global_load_lds_dwordx4 v[110:111], off
	s_mov_b32 m0, s5
	v_lshl_add_u64 v[98:99], v[224:225], 0, s[62:63]
	s_addk_i32 s4, 0x400
	s_mov_b32 s5, m0
	s_mov_b32 m0, s4
	s_nop 0
	global_load_lds_dwordx4 v[98:99], off
	s_mov_b32 m0, s5
	v_max_f32_e32 v98, v82, v83
	v_max3_f32 v99, v84, v85, v67
	v_max3_f32 v98, v98, v66, v68
	v_max3_f32 v98, v98, v69, v86
	v_max3_f32 v99, v99, v88, v89
	v_max3_f32 v98, v98, v87, v70
	v_max3_f32 v99, v99, v72, v73
	v_max3_f32 v98, v98, v71, v90
	v_max3_f32 v99, v99, v92, v93
	v_max3_f32 v98, v98, v91, v74
	v_max3_f32 v99, v99, v76, v77
	v_max3_f32 v98, v98, v75, v94
	v_max3_f32 v99, v99, v96, v97
	v_max3_f32 v98, v98, v95, v78
	v_max3_f32 v99, v99, v80, v81
	v_max3_f32 v98, v98, v79, v99
	v_mov_b32_e32 v99, v98
	s_nop 1
	v_permlane32_swap_b32_e32 v98, v99
	v_max_f32_e32 v98, v98, v99
	s_mov_b64 s[4:5], 0
	v_cmp_lt_f32_e32 vcc, s3, v98
	s_cbranch_vccnz .LBB0_1039

.LBB0_1036:
	v_max_f32_e32 v66, v66, v66
	v_max_f32_e32 v67, 0, v66
	v_exp_f32_e64 v66, -v67
	s_mov_b64 s[4:5], -1
	s_and_saveexec_b64 s[6:7], s[40:41]
	ds_write_b32 v205, v66
	s_or_b64 exec, exec, s[6:7]
	v_sub_f32_e32 v98, v98, v67
	v_sub_f32_e32 v99, v99, v67
	v_sub_f32_e32 v100, v100, v67
	v_sub_f32_e32 v101, v101, v67
	v_sub_f32_e32 v102, v102, v67
	v_sub_f32_e32 v103, v103, v67
	v_sub_f32_e32 v104, v104, v67
	v_sub_f32_e32 v105, v105, v67
	v_sub_f32_e32 v106, v106, v67
	v_sub_f32_e32 v107, v107, v67
	v_sub_f32_e32 v108, v108, v67
	v_sub_f32_e32 v109, v109, v67
	v_sub_f32_e32 v110, v110, v67
	v_sub_f32_e32 v111, v111, v67
	v_sub_f32_e32 v112, v112, v67
	v_sub_f32_e32 v113, v113, v67
	v_sub_f32_e32 v114, v114, v67
	v_sub_f32_e32 v115, v115, v67
	v_sub_f32_e32 v116, v116, v67
	v_sub_f32_e32 v117, v117, v67
	v_sub_f32_e32 v118, v118, v67
	v_sub_f32_e32 v119, v119, v67
	v_sub_f32_e32 v120, v120, v67
	v_sub_f32_e32 v121, v121, v67
	v_sub_f32_e32 v122, v122, v67
	v_sub_f32_e32 v123, v123, v67
	v_sub_f32_e32 v124, v124, v67
	v_sub_f32_e32 v125, v125, v67
	v_sub_f32_e32 v126, v126, v67
	v_sub_f32_e32 v127, v127, v67
	v_sub_f32_e32 v128, v128, v67
	v_sub_f32_e32 v129, v129, v67
	v_add_f32_e32 v207, v207, v67
	v_sub_f32_e32 v236, 0, v207
	v_sub_f32_e32 v237, 0, v207
	v_sub_f32_e32 v238, 0, v207
	v_sub_f32_e32 v239, 0, v207
	v_sub_f32_e32 v240, 0, v207
	v_sub_f32_e32 v241, 0, v207
	v_sub_f32_e32 v242, 0, v207
	v_sub_f32_e32 v243, 0, v207
	v_sub_f32_e32 v244, 0, v207
	v_sub_f32_e32 v245, 0, v207
	v_sub_f32_e32 v246, 0, v207
	v_sub_f32_e32 v247, 0, v207
	v_sub_f32_e32 v248, 0, v207
	v_sub_f32_e32 v249, 0, v207
	v_sub_f32_e32 v250, 0, v207
	v_sub_f32_e32 v251, 0, v207
	v_mul_f32_e32 v234, v234, v66
	s_branch .LBB0_1029
.LBB0_1039:
	v_max_f32_e32 v98, v98, v98
	v_max_f32_e32 v99, 0, v98
	v_exp_f32_e64 v98, -v99
	s_mov_b64 s[4:5], -1
	s_and_saveexec_b64 s[6:7], s[40:41]
	ds_write_b32 v205, v98
	s_or_b64 exec, exec, s[6:7]
	v_sub_f32_e32 v66, v66, v99
	v_sub_f32_e32 v67, v67, v99
	v_sub_f32_e32 v68, v68, v99
	v_sub_f32_e32 v69, v69, v99
	v_sub_f32_e32 v70, v70, v99
	v_sub_f32_e32 v71, v71, v99
	v_sub_f32_e32 v72, v72, v99
	v_sub_f32_e32 v73, v73, v99
	v_sub_f32_e32 v74, v74, v99
	v_sub_f32_e32 v75, v75, v99
	v_sub_f32_e32 v76, v76, v99
	v_sub_f32_e32 v77, v77, v99
	v_sub_f32_e32 v78, v78, v99
	v_sub_f32_e32 v79, v79, v99
	v_sub_f32_e32 v80, v80, v99
	v_sub_f32_e32 v81, v81, v99
	v_sub_f32_e32 v82, v82, v99
	v_sub_f32_e32 v83, v83, v99
	v_sub_f32_e32 v84, v84, v99
	v_sub_f32_e32 v85, v85, v99
	v_sub_f32_e32 v86, v86, v99
	v_sub_f32_e32 v87, v87, v99
	v_sub_f32_e32 v88, v88, v99
	v_sub_f32_e32 v89, v89, v99
	v_sub_f32_e32 v90, v90, v99
	v_sub_f32_e32 v91, v91, v99
	v_sub_f32_e32 v92, v92, v99
	v_sub_f32_e32 v93, v93, v99
	v_sub_f32_e32 v94, v94, v99
	v_sub_f32_e32 v95, v95, v99
	v_sub_f32_e32 v96, v96, v99
	v_sub_f32_e32 v97, v97, v99
	v_add_f32_e32 v207, v207, v99
	v_sub_f32_e32 v236, 0, v207
	v_sub_f32_e32 v237, 0, v207
	v_sub_f32_e32 v238, 0, v207
	v_sub_f32_e32 v239, 0, v207
	v_sub_f32_e32 v240, 0, v207
	v_sub_f32_e32 v241, 0, v207
	v_sub_f32_e32 v242, 0, v207
	v_sub_f32_e32 v243, 0, v207
	v_sub_f32_e32 v244, 0, v207
	v_sub_f32_e32 v245, 0, v207
	v_sub_f32_e32 v246, 0, v207
	v_sub_f32_e32 v247, 0, v207
	v_sub_f32_e32 v248, 0, v207
	v_sub_f32_e32 v249, 0, v207
	v_sub_f32_e32 v250, 0, v207
	v_sub_f32_e32 v251, 0, v207
	v_mul_f32_e32 v234, v234, v98
	s_branch .LBB0_1032
